# baseline (speedup 1.0000x reference)
_ZN12_GLOBAL__N_14k_fcEPKtPKiS1_PKfS5_Pf:
	s_load_dwordx8 s[4:11], s[0:1], 0x0
	s_load_dwordx4 s[12:15], s[0:1], 0x20
	s_and_b32 s3, s2, 7
	s_lshr_b32 s20, s2, 3
	s_lshr_b32 s19, s20, 2
	s_lshl_b32 s3, s3, 3
	s_add_u32 s19, s19, s3
	s_and_b32 s20, s20, 3
	v_lshrrev_b32_e32 v1, 6, v0
	v_and_b32_e32 v12, 63, v0
	v_and_b32_e32 v13, 15, v0
	v_readfirstlane_b32 s16, v1
	v_lshrrev_b32_e32 v14, 4, v12
	s_nop 3
	s_lshr_b32 s17, s16, 2
	s_and_b32 s18, s16, 3
	v_lshrrev_b32_e32 v70, 2, v12
	s_lshl_b32 s90, s19, 8
	s_lshl_b32 s91, s16, 5
	s_add_u32 s90, s90, s91
	v_add_u32_e32 v73, s90, v70
	v_add_u32_e32 v74, 16, v73
	v_lshlrev_b32_e32 v75, 3, v73
	v_lshlrev_b32_e32 v76, 3, v74
	s_waitcnt lgkmcnt(0)
	global_load_dwordx2 v[64:65], v75, s[6:7]
	global_load_dwordx2 v[66:67], v76, s[6:7]
	s_mul_i32 s90, s20, 0x180
	s_mul_i32 s91, s18, 96
	s_add_u32 s90, s90, s91
	v_lshl_add_u32 v15, v14, 2, s90
	v_lshlrev_b32_e32 v15, 2, v15
	global_load_dwordx4 v[16:19], v15, s[10:11] offset:0
	global_load_dwordx4 v[20:23], v15, s[10:11] offset:64
	global_load_dwordx4 v[24:27], v15, s[10:11] offset:128
	global_load_dwordx4 v[28:31], v15, s[10:11] offset:192
	global_load_dwordx4 v[32:35], v15, s[10:11] offset:256
	global_load_dwordx4 v[36:39], v15, s[10:11] offset:320
	v_mul_u32_u24_e32 v77, 0x1800, v13
	v_add_u32_e32 v77, v77, v15
	v_mov_b32_e32 v40, 0
	v_mov_b32_e32 v41, 0
	v_mov_b32_e32 v42, 0
	v_mov_b32_e32 v43, 0
	v_mov_b32_e32 v44, 0
	v_mov_b32_e32 v45, 0
	v_mov_b32_e32 v46, 0
	v_mov_b32_e32 v47, 0
	v_mov_b32_e32 v48, 0
	v_mov_b32_e32 v49, 0
	v_mov_b32_e32 v50, 0
	v_mov_b32_e32 v51, 0
	v_mov_b32_e32 v52, 0
	v_mov_b32_e32 v53, 0
	v_mov_b32_e32 v54, 0
	v_mov_b32_e32 v55, 0
	v_mov_b32_e32 v56, 0
	v_mov_b32_e32 v57, 0
	v_mov_b32_e32 v58, 0
	v_mov_b32_e32 v59, 0
	v_mov_b32_e32 v60, 0
	v_mov_b32_e32 v61, 0
	v_mov_b32_e32 v62, 0
	v_mov_b32_e32 v63, 0
	s_mov_b32 exec_lo, 0xff00ff
	s_mov_b32 exec_hi, 0xff00ff
	global_load_dwordx4 v[40:43], v77, s[12:13] offset:0
	global_load_dwordx4 v[44:47], v77, s[12:13] offset:64
	global_load_dwordx4 v[48:51], v77, s[12:13] offset:128
	global_load_dwordx4 v[52:55], v77, s[12:13] offset:192
	global_load_dwordx4 v[56:59], v77, s[12:13] offset:256
	global_load_dwordx4 v[60:63], v77, s[12:13] offset:320
	s_mov_b64 exec, -1
	v_lshlrev_b32_e32 v15, 6, v13
	v_lshl_add_u32 v15, v14, 4, v15
	v_lshrrev_b32_e32 v78, 3, v13
	v_lshlrev_b32_e32 v78, 5, v78
	v_xor_b32_e32 v15, v15, v78
	s_lshl_b32 s90, s17, 13
	v_add_u32_e32 v1, s90, v15
	v_add_u32_e32 v2, 0x14000, v1
	s_mul_i32 s90, s18, 0x1800
	s_add_u32 s90, s90, 0x4000
	v_add_u32_e32 v3, s90, v15
	v_add_u32_e32 v4, 0x14000, v3
	v_and_b32_e32 v71, 3, v12
	v_lshrrev_b32_e32 v72, 5, v12
	v_lshlrev_b32_e32 v72, 1, v72
	v_xor_b32_e32 v71, v71, v72
	v_lshlrev_b32_e32 v71, 4, v71
	v_lshl_add_u32 v11, v70, 6, v71
	s_mul_i32 s90, s20, 0x180
	s_mul_i32 s91, s16, 48
	s_add_u32 s90, s90, s91
	s_lshl_b32 s90, s90, 6
	s_add_u32 s28, s8, s90
	s_addc_u32 s29, s9, 0
	s_add_u32 s30, s28, 0x18000
	s_addc_u32 s31, s29, 0
	s_add_u32 s32, s28, 0x400
	s_addc_u32 s33, s29, 0
	s_add_u32 s34, s32, 0x18000
	s_addc_u32 s35, s33, 0
	s_add_u32 s36, s28, 0x800
	s_addc_u32 s37, s29, 0
	s_add_u32 s38, s36, 0x18000
	s_addc_u32 s39, s37, 0
	s_mov_b64 s[24:25], s[4:5]
	s_add_u32 s26, s4, 0x40
	s_addc_u32 s27, s5, 0
	s_add_u32 s96, s4, 0x1000000
	s_addc_u32 s97, s5, 0
	s_lshl_b32 s22, s16, 11
	s_mul_i32 s23, s16, 0xc00
	s_add_u32 s23, s23, 0x4000
	s_mov_b32 s21, 0
	s_lshr_b32 s92, s19, 1
	s_lshl_b32 s92, s92, 9
	s_movk_i32 s93, 0x1ff
	s_movk_i32 s94, 0x200
	v_lshl_add_u32 v5, v73, 10, v71
	v_lshl_add_u32 v6, v74, 10, v71
	s_add_u32 s24, s24, 0x1000000
	s_addc_u32 s25, s25, 0
	s_add_u32 s26, s26, 0x1000000
	s_addc_u32 s27, s27, 0
	s_add_u32 s28, s28, 0x180000
	s_addc_u32 s29, s29, 0
	s_add_u32 s30, s30, 0x180000
	s_addc_u32 s31, s31, 0
	s_add_u32 s32, s32, 0x180000
	s_addc_u32 s33, s33, 0
	s_add_u32 s34, s34, 0x180000
	s_addc_u32 s35, s35, 0
	s_add_u32 s36, s36, 0x180000
	s_addc_u32 s37, s37, 0
	s_add_u32 s38, s38, 0x180000
	s_addc_u32 s39, s39, 0
	s_cmp_lg_u32 s17, 0
	s_cbranch_scc1 .Lfc_h1_entry
	s_add_u32 m0, s22, 0x0
	s_nop 0
	global_load_lds_dwordx4 v5, s[24:25]
	s_add_u32 m0, s22, 0x400
	s_nop 0
	global_load_lds_dwordx4 v6, s[24:25]
	s_add_u32 m0, s23, 0x0
	s_nop 0
	global_load_lds_dwordx4 v11, s[28:29]
	s_add_u32 m0, s23, 0x400
	s_nop 0
	global_load_lds_dwordx4 v11, s[32:33]
	s_add_u32 m0, s23, 0x800
	s_nop 0
	global_load_lds_dwordx4 v11, s[36:37]
	s_add_u32 s24, s24, 0x80
	s_addc_u32 s25, s25, 0
	s_add_u32 s28, s28, 0x30000
	s_addc_u32 s29, s29, 0
	s_add_u32 s32, s32, 0x30000
	s_addc_u32 s33, s33, 0
	s_add_u32 s36, s36, 0x30000
	s_addc_u32 s37, s37, 0
	s_add_u32 m0, s22, 0xa000
	s_nop 0
	global_load_lds_dwordx4 v5, s[26:27]
	s_add_u32 m0, s22, 0xa400
	s_nop 0
	global_load_lds_dwordx4 v6, s[26:27]
	s_add_u32 m0, s23, 0xa000
	s_nop 0
	global_load_lds_dwordx4 v11, s[30:31]
	s_add_u32 m0, s23, 0xa400
	s_nop 0
	global_load_lds_dwordx4 v11, s[34:35]
	s_add_u32 m0, s23, 0xa800
	s_nop 0
	global_load_lds_dwordx4 v11, s[38:39]
	s_add_u32 s26, s26, 0x80
	s_addc_u32 s27, s27, 0
	s_add_u32 s30, s30, 0x30000
	s_addc_u32 s31, s31, 0
	s_add_u32 s34, s34, 0x30000
	s_addc_u32 s35, s35, 0
	s_add_u32 s38, s38, 0x30000
	s_addc_u32 s39, s39, 0
	s_add_u32 m0, s22, 0x14000
	s_nop 0
	global_load_lds_dwordx4 v5, s[24:25]
	s_add_u32 m0, s22, 0x14400
	s_nop 0
	global_load_lds_dwordx4 v6, s[24:25]
	s_add_u32 m0, s23, 0x14000
	s_nop 0
	global_load_lds_dwordx4 v11, s[28:29]
	s_add_u32 m0, s23, 0x14400
	s_nop 0
	global_load_lds_dwordx4 v11, s[32:33]
	s_add_u32 m0, s23, 0x14800
	s_nop 0
	global_load_lds_dwordx4 v11, s[36:37]
	s_add_u32 s24, s24, 0x80
	s_addc_u32 s25, s25, 0
	s_add_u32 s28, s28, 0x30000
	s_addc_u32 s29, s29, 0
	s_add_u32 s32, s32, 0x30000
	s_addc_u32 s33, s33, 0
	s_add_u32 s36, s36, 0x30000
	s_addc_u32 s37, s37, 0
	s_add_u32 m0, s22, 0x1e000
	s_nop 0
	global_load_lds_dwordx4 v5, s[26:27]
	s_add_u32 m0, s22, 0x1e400
	s_nop 0
	global_load_lds_dwordx4 v6, s[26:27]
	s_add_u32 m0, s23, 0x1e000
	s_nop 0
	global_load_lds_dwordx4 v11, s[30:31]
	s_add_u32 m0, s23, 0x1e400
	s_nop 0
	global_load_lds_dwordx4 v11, s[34:35]
	s_add_u32 m0, s23, 0x1e800
	s_nop 0
	global_load_lds_dwordx4 v11, s[38:39]
	s_add_u32 s26, s26, 0x80
	s_addc_u32 s27, s27, 0
	s_add_u32 s30, s30, 0x30000
	s_addc_u32 s31, s31, 0
	s_add_u32 s34, s34, 0x30000
	s_addc_u32 s35, s35, 0
	s_add_u32 s38, s38, 0x30000
	s_addc_u32 s39, s39, 0
	s_waitcnt vmcnt(20)
	v_med3_i32 v64, v64, 0, s93
	v_med3_i32 v65, v65, 1, s94
	v_med3_i32 v66, v66, 0, s93
	v_med3_i32 v67, v67, 1, s94
	v_add_u32_e32 v64, s92, v64
	v_add_u32_e32 v66, s92, v66
	v_add_u32_e32 v65, s92, v65
	v_add_u32_e32 v67, s92, v67
	v_add_u32_e32 v65, -1, v65
	v_add_u32_e32 v67, -1, v67
	v_lshl_add_u32 v7, v64, 10, v71
	v_lshl_add_u32 v8, v66, 10, v71
	v_lshl_add_u32 v9, v65, 10, v71
	v_lshl_add_u32 v10, v67, 10, v71
	v_cvt_pk_f16_f32 v12, v40, v41
	v_cvt_pk_f16_f32 v13, v42, v43
	v_cvt_pk_f16_f32 v14, v44, v45
	v_cvt_pk_f16_f32 v15, v46, v47
	v_cvt_pk_f16_f32 v56, v56, v57
	v_cvt_pk_f16_f32 v57, v58, v59
	v_cvt_pk_f16_f32 v58, v60, v61
	v_cvt_pk_f16_f32 v59, v62, v63
	v_cvt_pk_f16_f32 v60, v48, v49
	v_cvt_pk_f16_f32 v61, v50, v51
	v_cvt_pk_f16_f32 v62, v52, v53
	v_cvt_pk_f16_f32 v63, v54, v55
	v_mov_b32_e32 v64, v16
	v_mov_b32_e32 v65, v17
	v_mov_b32_e32 v66, v18
	v_mov_b32_e32 v67, v19
	v_mov_b32_e32 v68, v20
	v_mov_b32_e32 v69, v21
	v_mov_b32_e32 v70, v22
	v_mov_b32_e32 v71, v23
	v_mov_b32_e32 v72, v24
	v_mov_b32_e32 v73, v25
	v_mov_b32_e32 v74, v26
	v_mov_b32_e32 v75, v27
	v_mov_b32_e32 v76, v28
	v_mov_b32_e32 v77, v29
	v_mov_b32_e32 v78, v30
	v_mov_b32_e32 v79, v31
	v_mov_b32_e32 v80, v32
	v_mov_b32_e32 v81, v33
	v_mov_b32_e32 v82, v34
	v_mov_b32_e32 v83, v35
	v_mov_b32_e32 v84, v36
	v_mov_b32_e32 v85, v37
	v_mov_b32_e32 v86, v38
	v_mov_b32_e32 v87, v39
	v_mov_b32_e32 v88, v16
	v_mov_b32_e32 v89, v17
	v_mov_b32_e32 v90, v18
	v_mov_b32_e32 v91, v19
	v_mov_b32_e32 v92, v20
	v_mov_b32_e32 v93, v21
	v_mov_b32_e32 v94, v22
	v_mov_b32_e32 v95, v23
	v_mov_b32_e32 v96, v24
	v_mov_b32_e32 v97, v25
	v_mov_b32_e32 v98, v26
	v_mov_b32_e32 v99, v27
	v_mov_b32_e32 v100, v28
	v_mov_b32_e32 v101, v29
	v_mov_b32_e32 v102, v30
	v_mov_b32_e32 v103, v31
	v_mov_b32_e32 v104, v32
	v_mov_b32_e32 v105, v33
	v_mov_b32_e32 v106, v34
	v_mov_b32_e32 v107, v35
	v_mov_b32_e32 v108, v36
	v_mov_b32_e32 v109, v37
	v_mov_b32_e32 v110, v38
	v_mov_b32_e32 v111, v39
	v_mov_b32_e32 v112, v16
	v_mov_b32_e32 v113, v17
	v_mov_b32_e32 v114, v18
	v_mov_b32_e32 v115, v19
	v_mov_b32_e32 v116, v20
	v_mov_b32_e32 v117, v21
	v_mov_b32_e32 v118, v22
	v_mov_b32_e32 v119, v23
	v_mov_b32_e32 v120, v24
	v_mov_b32_e32 v121, v25
	v_mov_b32_e32 v122, v26
	v_mov_b32_e32 v123, v27
	v_mov_b32_e32 v124, v28
	v_mov_b32_e32 v125, v29
	v_mov_b32_e32 v126, v30
	v_mov_b32_e32 v127, v31
	v_mov_b32_e32 v128, v32
	v_mov_b32_e32 v129, v33
	v_mov_b32_e32 v130, v34
	v_mov_b32_e32 v131, v35
	v_mov_b32_e32 v132, v36
	v_mov_b32_e32 v133, v37
	v_mov_b32_e32 v134, v38
	v_mov_b32_e32 v135, v39
	v_mov_b32_e32 v136, v16
	v_mov_b32_e32 v137, v17
	v_mov_b32_e32 v138, v18
	v_mov_b32_e32 v139, v19
	v_mov_b32_e32 v140, v20
	v_mov_b32_e32 v141, v21
	v_mov_b32_e32 v142, v22
	v_mov_b32_e32 v143, v23
	v_mov_b32_e32 v144, v24
	v_mov_b32_e32 v145, v25
	v_mov_b32_e32 v146, v26
	v_mov_b32_e32 v147, v27
	v_mov_b32_e32 v148, v28
	v_mov_b32_e32 v149, v29
	v_mov_b32_e32 v150, v30
	v_mov_b32_e32 v151, v31
	v_mov_b32_e32 v152, v32
	v_mov_b32_e32 v153, v33
	v_mov_b32_e32 v154, v34
	v_mov_b32_e32 v155, v35
	v_mov_b32_e32 v156, v36
	v_mov_b32_e32 v157, v37
	v_mov_b32_e32 v158, v38
	v_mov_b32_e32 v159, v39
	v_mov_b32_e32 v160, v16
	v_mov_b32_e32 v161, v17
	v_mov_b32_e32 v162, v18
	v_mov_b32_e32 v163, v19
	v_mov_b32_e32 v164, v20
	v_mov_b32_e32 v165, v21
	v_mov_b32_e32 v166, v22
	v_mov_b32_e32 v167, v23
	v_mov_b32_e32 v168, v24
	v_mov_b32_e32 v169, v25
	v_mov_b32_e32 v170, v26
	v_mov_b32_e32 v171, v27
	v_mov_b32_e32 v172, v28
	v_mov_b32_e32 v173, v29
	v_mov_b32_e32 v174, v30
	v_mov_b32_e32 v175, v31
	v_mov_b32_e32 v176, v32
	v_mov_b32_e32 v177, v33
	v_mov_b32_e32 v178, v34
	v_mov_b32_e32 v179, v35
	v_mov_b32_e32 v180, v36
	v_mov_b32_e32 v181, v37
	v_mov_b32_e32 v182, v38
	v_mov_b32_e32 v183, v39
	v_mov_b32_e32 v184, v16
	v_mov_b32_e32 v185, v17
	v_mov_b32_e32 v186, v18
	v_mov_b32_e32 v187, v19
	v_mov_b32_e32 v188, v20
	v_mov_b32_e32 v189, v21
	v_mov_b32_e32 v190, v22
	v_mov_b32_e32 v191, v23
	v_mov_b32_e32 v192, v24
	v_mov_b32_e32 v193, v25
	v_mov_b32_e32 v194, v26
	v_mov_b32_e32 v195, v27
	v_mov_b32_e32 v196, v28
	v_mov_b32_e32 v197, v29
	v_mov_b32_e32 v198, v30
	v_mov_b32_e32 v199, v31
	v_mov_b32_e32 v200, v32
	v_mov_b32_e32 v201, v33
	v_mov_b32_e32 v202, v34
	v_mov_b32_e32 v203, v35
	v_mov_b32_e32 v204, v36
	v_mov_b32_e32 v205, v37
	v_mov_b32_e32 v206, v38
	v_mov_b32_e32 v207, v39
	v_mov_b32_e32 v208, v16
	v_mov_b32_e32 v209, v17
	v_mov_b32_e32 v210, v18
	v_mov_b32_e32 v211, v19
	v_mov_b32_e32 v212, v20
	v_mov_b32_e32 v213, v21
	v_mov_b32_e32 v214, v22
	v_mov_b32_e32 v215, v23
	v_mov_b32_e32 v216, v24
	v_mov_b32_e32 v217, v25
	v_mov_b32_e32 v218, v26
	v_mov_b32_e32 v219, v27
	v_mov_b32_e32 v220, v28
	v_mov_b32_e32 v221, v29
	v_mov_b32_e32 v222, v30
	v_mov_b32_e32 v223, v31
	v_mov_b32_e32 v224, v32
	v_mov_b32_e32 v225, v33
	v_mov_b32_e32 v226, v34
	v_mov_b32_e32 v227, v35
	v_mov_b32_e32 v228, v36
	v_mov_b32_e32 v229, v37
	v_mov_b32_e32 v230, v38
	v_mov_b32_e32 v231, v39
	v_mov_b32_e32 v232, v16
	v_mov_b32_e32 v233, v17
	v_mov_b32_e32 v234, v18
	v_mov_b32_e32 v235, v19
	v_mov_b32_e32 v236, v20
	v_mov_b32_e32 v237, v21
	v_mov_b32_e32 v238, v22
	v_mov_b32_e32 v239, v23
	v_mov_b32_e32 v240, v24
	v_mov_b32_e32 v241, v25
	v_mov_b32_e32 v242, v26
	v_mov_b32_e32 v243, v27
	v_mov_b32_e32 v244, v28
	v_mov_b32_e32 v245, v29
	v_mov_b32_e32 v246, v30
	v_mov_b32_e32 v247, v31
	v_mov_b32_e32 v248, v32
	v_mov_b32_e32 v249, v33
	v_mov_b32_e32 v250, v34
	v_mov_b32_e32 v251, v35
	v_mov_b32_e32 v252, v36
	v_mov_b32_e32 v253, v37
	v_mov_b32_e32 v254, v38
	v_mov_b32_e32 v255, v39
	s_waitcnt vmcnt(15)
	s_barrier

.Lfc_ng_1:
	s_barrier
	s_waitcnt lgkmcnt(0)
	v_mfma_f32_16x16x32_f16 v[64:67], v[16:19], v[40:43], v[64:67]
	v_mfma_f32_16x16x32_f16 v[68:71], v[20:23], v[40:43], v[68:71]
	v_mfma_f32_16x16x32_f16 v[72:75], v[24:27], v[40:43], v[72:75]
	v_mfma_f32_16x16x32_f16 v[76:79], v[28:31], v[40:43], v[76:79]
	v_mfma_f32_16x16x32_f16 v[80:83], v[32:35], v[40:43], v[80:83]
	v_mfma_f32_16x16x32_f16 v[84:87], v[36:39], v[40:43], v[84:87]
	v_mfma_f32_16x16x32_f16 v[88:91], v[16:19], v[44:47], v[88:91]
	ds_read_b128 v[40:43], v1 offset:4096
	v_mfma_f32_16x16x32_f16 v[92:95], v[20:23], v[44:47], v[92:95]
	v_mfma_f32_16x16x32_f16 v[96:99], v[24:27], v[44:47], v[96:99]
	v_mfma_f32_16x16x32_f16 v[100:103], v[28:31], v[44:47], v[100:103]
	v_mfma_f32_16x16x32_f16 v[104:107], v[32:35], v[44:47], v[104:107]
	v_mfma_f32_16x16x32_f16 v[108:111], v[36:39], v[44:47], v[108:111]
	v_mfma_f32_16x16x32_f16 v[112:115], v[16:19], v[48:51], v[112:115]
	ds_read_b128 v[44:47], v1 offset:5120
	v_mfma_f32_16x16x32_f16 v[116:119], v[20:23], v[48:51], v[116:119]
	v_mfma_f32_16x16x32_f16 v[120:123], v[24:27], v[48:51], v[120:123]
	v_mfma_f32_16x16x32_f16 v[124:127], v[28:31], v[48:51], v[124:127]
	v_mfma_f32_16x16x32_f16 v[128:131], v[32:35], v[48:51], v[128:131]
	v_mfma_f32_16x16x32_f16 v[132:135], v[36:39], v[48:51], v[132:135]
	v_mfma_f32_16x16x32_f16 v[136:139], v[16:19], v[52:55], v[136:139]
	ds_read_b128 v[48:51], v1 offset:6144
	v_mfma_f32_16x16x32_f16 v[140:143], v[20:23], v[52:55], v[140:143]
	v_mfma_f32_16x16x32_f16 v[144:147], v[24:27], v[52:55], v[144:147]
	v_mfma_f32_16x16x32_f16 v[148:151], v[28:31], v[52:55], v[148:151]
	v_mfma_f32_16x16x32_f16 v[152:155], v[32:35], v[52:55], v[152:155]
	v_mfma_f32_16x16x32_f16 v[156:159], v[36:39], v[52:55], v[156:159]
	s_waitcnt lgkmcnt(2)
	v_mfma_f32_16x16x32_f16 v[160:163], v[16:19], v[40:43], v[160:163]
	ds_read_b128 v[52:55], v1 offset:7168
	v_mfma_f32_16x16x32_f16 v[164:167], v[20:23], v[40:43], v[164:167]
	v_mfma_f32_16x16x32_f16 v[168:171], v[24:27], v[40:43], v[168:171]
	v_mfma_f32_16x16x32_f16 v[172:175], v[28:31], v[40:43], v[172:175]
	v_mfma_f32_16x16x32_f16 v[176:179], v[32:35], v[40:43], v[176:179]
	v_mfma_f32_16x16x32_f16 v[180:183], v[36:39], v[40:43], v[180:183]
	s_waitcnt lgkmcnt(2)
	v_mfma_f32_16x16x32_f16 v[184:187], v[16:19], v[44:47], v[184:187]
	v_mfma_f32_16x16x32_f16 v[188:191], v[20:23], v[44:47], v[188:191]
	v_mfma_f32_16x16x32_f16 v[192:195], v[24:27], v[44:47], v[192:195]
	v_mfma_f32_16x16x32_f16 v[196:199], v[28:31], v[44:47], v[196:199]
	v_mfma_f32_16x16x32_f16 v[200:203], v[32:35], v[44:47], v[200:203]
	v_mfma_f32_16x16x32_f16 v[204:207], v[36:39], v[44:47], v[204:207]
	s_cmp_eq_u32 s21, 11
	s_cbranch_scc1 .Lfc_w0_2
	s_waitcnt vmcnt(5)
	s_branch .Lfc_w1_2

.Lfc_w1_2:
	s_waitcnt lgkmcnt(1)
	v_mfma_f32_16x16x32_f16 v[208:211], v[16:19], v[48:51], v[208:211]
	v_mfma_f32_16x16x32_f16 v[212:215], v[20:23], v[48:51], v[212:215]
	v_mfma_f32_16x16x32_f16 v[216:219], v[24:27], v[48:51], v[216:219]
	v_mfma_f32_16x16x32_f16 v[220:223], v[28:31], v[48:51], v[220:223]
	v_mfma_f32_16x16x32_f16 v[224:227], v[32:35], v[48:51], v[224:227]
	v_mfma_f32_16x16x32_f16 v[228:231], v[36:39], v[48:51], v[228:231]
	s_waitcnt lgkmcnt(0)
	v_mfma_f32_16x16x32_f16 v[232:235], v[16:19], v[52:55], v[232:235]
	v_mfma_f32_16x16x32_f16 v[236:239], v[20:23], v[52:55], v[236:239]
	v_mfma_f32_16x16x32_f16 v[240:243], v[24:27], v[52:55], v[240:243]
	v_mfma_f32_16x16x32_f16 v[244:247], v[28:31], v[52:55], v[244:247]
	v_mfma_f32_16x16x32_f16 v[248:251], v[32:35], v[52:55], v[248:251]
	v_mfma_f32_16x16x32_f16 v[252:255], v[36:39], v[52:55], v[252:255]
	s_barrier
	ds_read_b128 v[16:19], v3 offset:40960
	ds_read_b128 v[20:23], v3 offset:41984
	ds_read_b128 v[24:27], v3 offset:43008
	ds_read_b128 v[28:31], v3 offset:44032
	ds_read_b128 v[32:35], v3 offset:45056
	ds_read_b128 v[36:39], v3 offset:46080
	ds_read_b128 v[40:43], v1 offset:40960
	ds_read_b128 v[44:47], v1 offset:41984
	ds_read_b128 v[48:51], v1 offset:43008
	ds_read_b128 v[52:55], v1 offset:44032
	s_cmp_eq_u32 s21, 0
	s_cbranch_scc1 .Lfc_ng_3
	s_add_u32 m0, s22, 0x1e000
	s_nop 0
	global_load_lds_dwordx4 v5, s[26:27]
	s_add_u32 m0, s22, 0x1e400
	s_nop 0
	global_load_lds_dwordx4 v6, s[26:27]
	s_add_u32 m0, s23, 0x1e000
	s_nop 0
	global_load_lds_dwordx4 v11, s[30:31]
	s_add_u32 m0, s23, 0x1e400
	s_nop 0
	global_load_lds_dwordx4 v11, s[34:35]
	s_add_u32 m0, s23, 0x1e800
	s_nop 0
	global_load_lds_dwordx4 v11, s[38:39]
	s_add_u32 s26, s26, 0x80
	s_addc_u32 s27, s27, 0
	s_add_u32 s30, s30, 0x30000
	s_addc_u32 s31, s31, 0
	s_add_u32 s34, s34, 0x30000
	s_addc_u32 s35, s35, 0
	s_add_u32 s38, s38, 0x30000
	s_addc_u32 s39, s39, 0
	s_cmp_eq_u32 s21, 3
	s_cbranch_scc1 .Lfc_sw_4
	s_cmp_eq_u32 s21, 7
	s_cbranch_scc0 .Lfc_swd_4
	s_add_u32 s28, s28, 0x180000
	s_addc_u32 s29, s29, 0
	s_add_u32 s30, s30, 0x180000
	s_addc_u32 s31, s31, 0
	s_add_u32 s32, s32, 0x180000
	s_addc_u32 s33, s33, 0
	s_add_u32 s34, s34, 0x180000
	s_addc_u32 s35, s35, 0
	s_add_u32 s36, s36, 0x180000
	s_addc_u32 s37, s37, 0
	s_add_u32 s38, s38, 0x180000
	s_addc_u32 s39, s39, 0
	s_branch .Lfc_sw2_4
.Lfc_sw_4:
	s_sub_u32 s28, s28, 0x300000
	s_subb_u32 s29, s29, 0
	s_sub_u32 s30, s30, 0x300000
	s_subb_u32 s31, s31, 0
	s_sub_u32 s32, s32, 0x300000
	s_subb_u32 s33, s33, 0
	s_sub_u32 s34, s34, 0x300000
	s_subb_u32 s35, s35, 0
	s_sub_u32 s36, s36, 0x300000
	s_subb_u32 s37, s37, 0
	s_sub_u32 s38, s38, 0x300000
	s_subb_u32 s39, s39, 0
.Lfc_sw2_4:
	s_mov_b64 s[24:25], s[4:5]
	s_add_u32 s26, s4, 0x40
	s_addc_u32 s27, s5, 0
	v_mov_b32_e32 v5, v7
	v_mov_b32_e32 v6, v8
	v_mov_b32_e32 v7, v9
	v_mov_b32_e32 v8, v10
.Lfc_swd_4:
.Lfc_ng_3:
	s_barrier
	s_waitcnt lgkmcnt(0)
	v_mfma_f32_16x16x32_f16 v[64:67], v[16:19], v[40:43], v[64:67]
	v_mfma_f32_16x16x32_f16 v[68:71], v[20:23], v[40:43], v[68:71]
	v_mfma_f32_16x16x32_f16 v[72:75], v[24:27], v[40:43], v[72:75]
	v_mfma_f32_16x16x32_f16 v[76:79], v[28:31], v[40:43], v[76:79]
	v_mfma_f32_16x16x32_f16 v[80:83], v[32:35], v[40:43], v[80:83]
	v_mfma_f32_16x16x32_f16 v[84:87], v[36:39], v[40:43], v[84:87]
	v_mfma_f32_16x16x32_f16 v[88:91], v[16:19], v[44:47], v[88:91]
	ds_read_b128 v[40:43], v1 offset:45056
	v_mfma_f32_16x16x32_f16 v[92:95], v[20:23], v[44:47], v[92:95]
	v_mfma_f32_16x16x32_f16 v[96:99], v[24:27], v[44:47], v[96:99]
	v_mfma_f32_16x16x32_f16 v[100:103], v[28:31], v[44:47], v[100:103]
	v_mfma_f32_16x16x32_f16 v[104:107], v[32:35], v[44:47], v[104:107]
	v_mfma_f32_16x16x32_f16 v[108:111], v[36:39], v[44:47], v[108:111]
	v_mfma_f32_16x16x32_f16 v[112:115], v[16:19], v[48:51], v[112:115]
	ds_read_b128 v[44:47], v1 offset:46080
	v_mfma_f32_16x16x32_f16 v[116:119], v[20:23], v[48:51], v[116:119]
	v_mfma_f32_16x16x32_f16 v[120:123], v[24:27], v[48:51], v[120:123]
	v_mfma_f32_16x16x32_f16 v[124:127], v[28:31], v[48:51], v[124:127]
	v_mfma_f32_16x16x32_f16 v[128:131], v[32:35], v[48:51], v[128:131]
	v_mfma_f32_16x16x32_f16 v[132:135], v[36:39], v[48:51], v[132:135]
	v_mfma_f32_16x16x32_f16 v[136:139], v[16:19], v[52:55], v[136:139]
	ds_read_b128 v[48:51], v1 offset:47104
	v_mfma_f32_16x16x32_f16 v[140:143], v[20:23], v[52:55], v[140:143]
	v_mfma_f32_16x16x32_f16 v[144:147], v[24:27], v[52:55], v[144:147]
	v_mfma_f32_16x16x32_f16 v[148:151], v[28:31], v[52:55], v[148:151]
	v_mfma_f32_16x16x32_f16 v[152:155], v[32:35], v[52:55], v[152:155]
	v_mfma_f32_16x16x32_f16 v[156:159], v[36:39], v[52:55], v[156:159]
	s_waitcnt lgkmcnt(2)
	v_mfma_f32_16x16x32_f16 v[160:163], v[16:19], v[40:43], v[160:163]
	ds_read_b128 v[52:55], v1 offset:48128
	v_mfma_f32_16x16x32_f16 v[164:167], v[20:23], v[40:43], v[164:167]
	v_mfma_f32_16x16x32_f16 v[168:171], v[24:27], v[40:43], v[168:171]
	v_mfma_f32_16x16x32_f16 v[172:175], v[28:31], v[40:43], v[172:175]
	v_mfma_f32_16x16x32_f16 v[176:179], v[32:35], v[40:43], v[176:179]
	v_mfma_f32_16x16x32_f16 v[180:183], v[36:39], v[40:43], v[180:183]
	s_waitcnt lgkmcnt(2)
	v_mfma_f32_16x16x32_f16 v[184:187], v[16:19], v[44:47], v[184:187]
	v_mfma_f32_16x16x32_f16 v[188:191], v[20:23], v[44:47], v[188:191]
	v_mfma_f32_16x16x32_f16 v[192:195], v[24:27], v[44:47], v[192:195]
	v_mfma_f32_16x16x32_f16 v[196:199], v[28:31], v[44:47], v[196:199]
	v_mfma_f32_16x16x32_f16 v[200:203], v[32:35], v[44:47], v[200:203]
	v_mfma_f32_16x16x32_f16 v[204:207], v[36:39], v[44:47], v[204:207]
	s_cmp_eq_u32 s21, 11
	s_cbranch_scc1 .Lfc_w0_5
	s_waitcnt vmcnt(5)
	s_branch .Lfc_w1_5

.Lfc_w1_5:
	s_waitcnt lgkmcnt(1)
	v_mfma_f32_16x16x32_f16 v[208:211], v[16:19], v[48:51], v[208:211]
	v_mfma_f32_16x16x32_f16 v[212:215], v[20:23], v[48:51], v[212:215]
	v_mfma_f32_16x16x32_f16 v[216:219], v[24:27], v[48:51], v[216:219]
	v_mfma_f32_16x16x32_f16 v[220:223], v[28:31], v[48:51], v[220:223]
	v_mfma_f32_16x16x32_f16 v[224:227], v[32:35], v[48:51], v[224:227]
	v_mfma_f32_16x16x32_f16 v[228:231], v[36:39], v[48:51], v[228:231]
	s_waitcnt lgkmcnt(0)
	v_mfma_f32_16x16x32_f16 v[232:235], v[16:19], v[52:55], v[232:235]
	v_mfma_f32_16x16x32_f16 v[236:239], v[20:23], v[52:55], v[236:239]
	v_mfma_f32_16x16x32_f16 v[240:243], v[24:27], v[52:55], v[240:243]
	v_mfma_f32_16x16x32_f16 v[244:247], v[28:31], v[52:55], v[244:247]
	v_mfma_f32_16x16x32_f16 v[248:251], v[32:35], v[52:55], v[248:251]
	v_mfma_f32_16x16x32_f16 v[252:255], v[36:39], v[52:55], v[252:255]
	s_barrier
	ds_read_b128 v[16:19], v4 offset:0
	ds_read_b128 v[20:23], v4 offset:1024
	ds_read_b128 v[24:27], v4 offset:2048
	ds_read_b128 v[28:31], v4 offset:3072
	ds_read_b128 v[32:35], v4 offset:4096
	ds_read_b128 v[36:39], v4 offset:5120
	ds_read_b128 v[40:43], v2 offset:0
	ds_read_b128 v[44:47], v2 offset:1024
	ds_read_b128 v[48:51], v2 offset:2048
	ds_read_b128 v[52:55], v2 offset:3072
	s_cmp_eq_u32 s21, 11
	s_cbranch_scc1 .Lfc_ng_6
	s_add_u32 m0, s22, 0x0
	s_nop 0
	global_load_lds_dwordx4 v5, s[24:25]
	s_add_u32 m0, s22, 0x400
	s_nop 0
	global_load_lds_dwordx4 v6, s[24:25]
	s_add_u32 m0, s23, 0x0
	s_nop 0
	global_load_lds_dwordx4 v11, s[28:29]
	s_add_u32 m0, s23, 0x400
	s_nop 0
	global_load_lds_dwordx4 v11, s[32:33]
	s_add_u32 m0, s23, 0x800
	s_nop 0
	global_load_lds_dwordx4 v11, s[36:37]
	s_add_u32 s24, s24, 0x80
	s_addc_u32 s25, s25, 0
	s_add_u32 s28, s28, 0x30000
	s_addc_u32 s29, s29, 0
	s_add_u32 s32, s32, 0x30000
	s_addc_u32 s33, s33, 0
	s_add_u32 s36, s36, 0x30000
	s_addc_u32 s37, s37, 0
.Lfc_ng_6:
	s_barrier
	s_waitcnt lgkmcnt(0)
	v_mfma_f32_16x16x32_f16 v[64:67], v[16:19], v[40:43], v[64:67]
	v_mfma_f32_16x16x32_f16 v[68:71], v[20:23], v[40:43], v[68:71]
	v_mfma_f32_16x16x32_f16 v[72:75], v[24:27], v[40:43], v[72:75]
	v_mfma_f32_16x16x32_f16 v[76:79], v[28:31], v[40:43], v[76:79]
	v_mfma_f32_16x16x32_f16 v[80:83], v[32:35], v[40:43], v[80:83]
	v_mfma_f32_16x16x32_f16 v[84:87], v[36:39], v[40:43], v[84:87]
	v_mfma_f32_16x16x32_f16 v[88:91], v[16:19], v[44:47], v[88:91]
	ds_read_b128 v[40:43], v2 offset:4096
	v_mfma_f32_16x16x32_f16 v[92:95], v[20:23], v[44:47], v[92:95]
	v_mfma_f32_16x16x32_f16 v[96:99], v[24:27], v[44:47], v[96:99]
	v_mfma_f32_16x16x32_f16 v[100:103], v[28:31], v[44:47], v[100:103]
	v_mfma_f32_16x16x32_f16 v[104:107], v[32:35], v[44:47], v[104:107]
	v_mfma_f32_16x16x32_f16 v[108:111], v[36:39], v[44:47], v[108:111]
	v_mfma_f32_16x16x32_f16 v[112:115], v[16:19], v[48:51], v[112:115]
	ds_read_b128 v[44:47], v2 offset:5120
	v_mfma_f32_16x16x32_f16 v[116:119], v[20:23], v[48:51], v[116:119]
	v_mfma_f32_16x16x32_f16 v[120:123], v[24:27], v[48:51], v[120:123]
	v_mfma_f32_16x16x32_f16 v[124:127], v[28:31], v[48:51], v[124:127]
	v_mfma_f32_16x16x32_f16 v[128:131], v[32:35], v[48:51], v[128:131]
	v_mfma_f32_16x16x32_f16 v[132:135], v[36:39], v[48:51], v[132:135]
	v_mfma_f32_16x16x32_f16 v[136:139], v[16:19], v[52:55], v[136:139]
	ds_read_b128 v[48:51], v2 offset:6144
	v_mfma_f32_16x16x32_f16 v[140:143], v[20:23], v[52:55], v[140:143]
	v_mfma_f32_16x16x32_f16 v[144:147], v[24:27], v[52:55], v[144:147]
	v_mfma_f32_16x16x32_f16 v[148:151], v[28:31], v[52:55], v[148:151]
	v_mfma_f32_16x16x32_f16 v[152:155], v[32:35], v[52:55], v[152:155]
	v_mfma_f32_16x16x32_f16 v[156:159], v[36:39], v[52:55], v[156:159]
	s_waitcnt lgkmcnt(2)
	v_mfma_f32_16x16x32_f16 v[160:163], v[16:19], v[40:43], v[160:163]
	ds_read_b128 v[52:55], v2 offset:7168
	v_mfma_f32_16x16x32_f16 v[164:167], v[20:23], v[40:43], v[164:167]
	v_mfma_f32_16x16x32_f16 v[168:171], v[24:27], v[40:43], v[168:171]
	v_mfma_f32_16x16x32_f16 v[172:175], v[28:31], v[40:43], v[172:175]
	v_mfma_f32_16x16x32_f16 v[176:179], v[32:35], v[40:43], v[176:179]
	v_mfma_f32_16x16x32_f16 v[180:183], v[36:39], v[40:43], v[180:183]
	s_waitcnt lgkmcnt(2)
	v_mfma_f32_16x16x32_f16 v[184:187], v[16:19], v[44:47], v[184:187]
	v_mfma_f32_16x16x32_f16 v[188:191], v[20:23], v[44:47], v[188:191]
	v_mfma_f32_16x16x32_f16 v[192:195], v[24:27], v[44:47], v[192:195]
	v_mfma_f32_16x16x32_f16 v[196:199], v[28:31], v[44:47], v[196:199]
	v_mfma_f32_16x16x32_f16 v[200:203], v[32:35], v[44:47], v[200:203]
	v_mfma_f32_16x16x32_f16 v[204:207], v[36:39], v[44:47], v[204:207]
	s_cmp_eq_u32 s21, 11
	s_cbranch_scc1 .Lfc_w0_7
	s_waitcnt vmcnt(5)
	s_branch .Lfc_w1_7

.Lfc_w1_7:
	s_waitcnt lgkmcnt(1)
	v_mfma_f32_16x16x32_f16 v[208:211], v[16:19], v[48:51], v[208:211]
	v_mfma_f32_16x16x32_f16 v[212:215], v[20:23], v[48:51], v[212:215]
	v_mfma_f32_16x16x32_f16 v[216:219], v[24:27], v[48:51], v[216:219]
	v_mfma_f32_16x16x32_f16 v[220:223], v[28:31], v[48:51], v[220:223]
	v_mfma_f32_16x16x32_f16 v[224:227], v[32:35], v[48:51], v[224:227]
	v_mfma_f32_16x16x32_f16 v[228:231], v[36:39], v[48:51], v[228:231]
	s_waitcnt lgkmcnt(0)
	v_mfma_f32_16x16x32_f16 v[232:235], v[16:19], v[52:55], v[232:235]
	v_mfma_f32_16x16x32_f16 v[236:239], v[20:23], v[52:55], v[236:239]
	v_mfma_f32_16x16x32_f16 v[240:243], v[24:27], v[52:55], v[240:243]
	v_mfma_f32_16x16x32_f16 v[244:247], v[28:31], v[52:55], v[244:247]
	v_mfma_f32_16x16x32_f16 v[248:251], v[32:35], v[52:55], v[248:251]
	v_mfma_f32_16x16x32_f16 v[252:255], v[36:39], v[52:55], v[252:255]
	s_barrier
	ds_read_b128 v[16:19], v4 offset:40960
	ds_read_b128 v[20:23], v4 offset:41984
	ds_read_b128 v[24:27], v4 offset:43008
	ds_read_b128 v[28:31], v4 offset:44032
	ds_read_b128 v[32:35], v4 offset:45056
	ds_read_b128 v[36:39], v4 offset:46080
	ds_read_b128 v[40:43], v2 offset:40960
	ds_read_b128 v[44:47], v2 offset:41984
	ds_read_b128 v[48:51], v2 offset:43008
	ds_read_b128 v[52:55], v2 offset:44032
	s_cmp_eq_u32 s21, 11
	s_cbranch_scc1 .Lfc_ng_8
	s_add_u32 m0, s22, 0xa000
	s_nop 0
	global_load_lds_dwordx4 v5, s[26:27]
	s_add_u32 m0, s22, 0xa400
	s_nop 0
	global_load_lds_dwordx4 v6, s[26:27]
	s_add_u32 m0, s23, 0xa000
	s_nop 0
	global_load_lds_dwordx4 v11, s[30:31]
	s_add_u32 m0, s23, 0xa400
	s_nop 0
	global_load_lds_dwordx4 v11, s[34:35]
	s_add_u32 m0, s23, 0xa800
	s_nop 0
	global_load_lds_dwordx4 v11, s[38:39]
	s_add_u32 s26, s26, 0x80
	s_addc_u32 s27, s27, 0
	s_add_u32 s30, s30, 0x30000
	s_addc_u32 s31, s31, 0
	s_add_u32 s34, s34, 0x30000
	s_addc_u32 s35, s35, 0
	s_add_u32 s38, s38, 0x30000
	s_addc_u32 s39, s39, 0
.Lfc_ng_8:
	s_barrier
	s_waitcnt lgkmcnt(0)
	v_mfma_f32_16x16x32_f16 v[64:67], v[16:19], v[40:43], v[64:67]
	v_mfma_f32_16x16x32_f16 v[68:71], v[20:23], v[40:43], v[68:71]
	v_mfma_f32_16x16x32_f16 v[72:75], v[24:27], v[40:43], v[72:75]
	v_mfma_f32_16x16x32_f16 v[76:79], v[28:31], v[40:43], v[76:79]
	v_mfma_f32_16x16x32_f16 v[80:83], v[32:35], v[40:43], v[80:83]
	v_mfma_f32_16x16x32_f16 v[84:87], v[36:39], v[40:43], v[84:87]
	v_mfma_f32_16x16x32_f16 v[88:91], v[16:19], v[44:47], v[88:91]
	ds_read_b128 v[40:43], v2 offset:45056
	v_mfma_f32_16x16x32_f16 v[92:95], v[20:23], v[44:47], v[92:95]
	v_mfma_f32_16x16x32_f16 v[96:99], v[24:27], v[44:47], v[96:99]
	v_mfma_f32_16x16x32_f16 v[100:103], v[28:31], v[44:47], v[100:103]
	v_mfma_f32_16x16x32_f16 v[104:107], v[32:35], v[44:47], v[104:107]
	v_mfma_f32_16x16x32_f16 v[108:111], v[36:39], v[44:47], v[108:111]
	v_mfma_f32_16x16x32_f16 v[112:115], v[16:19], v[48:51], v[112:115]
	ds_read_b128 v[44:47], v2 offset:46080
	v_mfma_f32_16x16x32_f16 v[116:119], v[20:23], v[48:51], v[116:119]
	v_mfma_f32_16x16x32_f16 v[120:123], v[24:27], v[48:51], v[120:123]
	v_mfma_f32_16x16x32_f16 v[124:127], v[28:31], v[48:51], v[124:127]
	v_mfma_f32_16x16x32_f16 v[128:131], v[32:35], v[48:51], v[128:131]
	v_mfma_f32_16x16x32_f16 v[132:135], v[36:39], v[48:51], v[132:135]
	v_mfma_f32_16x16x32_f16 v[136:139], v[16:19], v[52:55], v[136:139]
	ds_read_b128 v[48:51], v2 offset:47104
	v_mfma_f32_16x16x32_f16 v[140:143], v[20:23], v[52:55], v[140:143]
	v_mfma_f32_16x16x32_f16 v[144:147], v[24:27], v[52:55], v[144:147]
	v_mfma_f32_16x16x32_f16 v[148:151], v[28:31], v[52:55], v[148:151]
	v_mfma_f32_16x16x32_f16 v[152:155], v[32:35], v[52:55], v[152:155]
	v_mfma_f32_16x16x32_f16 v[156:159], v[36:39], v[52:55], v[156:159]
	s_waitcnt lgkmcnt(2)
	v_mfma_f32_16x16x32_f16 v[160:163], v[16:19], v[40:43], v[160:163]
	ds_read_b128 v[52:55], v2 offset:48128
	v_mfma_f32_16x16x32_f16 v[164:167], v[20:23], v[40:43], v[164:167]
	v_mfma_f32_16x16x32_f16 v[168:171], v[24:27], v[40:43], v[168:171]
	v_mfma_f32_16x16x32_f16 v[172:175], v[28:31], v[40:43], v[172:175]
	v_mfma_f32_16x16x32_f16 v[176:179], v[32:35], v[40:43], v[176:179]
	v_mfma_f32_16x16x32_f16 v[180:183], v[36:39], v[40:43], v[180:183]
	s_waitcnt lgkmcnt(2)
	v_mfma_f32_16x16x32_f16 v[184:187], v[16:19], v[44:47], v[184:187]
	v_mfma_f32_16x16x32_f16 v[188:191], v[20:23], v[44:47], v[188:191]
	v_mfma_f32_16x16x32_f16 v[192:195], v[24:27], v[44:47], v[192:195]
	v_mfma_f32_16x16x32_f16 v[196:199], v[28:31], v[44:47], v[196:199]
	v_mfma_f32_16x16x32_f16 v[200:203], v[32:35], v[44:47], v[200:203]
	v_mfma_f32_16x16x32_f16 v[204:207], v[36:39], v[44:47], v[204:207]
	s_cmp_eq_u32 s21, 11
	s_cbranch_scc1 .Lfc_w0_9
	s_waitcnt vmcnt(5)
	s_branch .Lfc_w1_9

.Lfc_w1_9:
	s_waitcnt lgkmcnt(1)
	v_mfma_f32_16x16x32_f16 v[208:211], v[16:19], v[48:51], v[208:211]
	v_mfma_f32_16x16x32_f16 v[212:215], v[20:23], v[48:51], v[212:215]
	v_mfma_f32_16x16x32_f16 v[216:219], v[24:27], v[48:51], v[216:219]
	v_mfma_f32_16x16x32_f16 v[220:223], v[28:31], v[48:51], v[220:223]
	v_mfma_f32_16x16x32_f16 v[224:227], v[32:35], v[48:51], v[224:227]
	v_mfma_f32_16x16x32_f16 v[228:231], v[36:39], v[48:51], v[228:231]
	s_waitcnt lgkmcnt(0)
	v_mfma_f32_16x16x32_f16 v[232:235], v[16:19], v[52:55], v[232:235]
	v_mfma_f32_16x16x32_f16 v[236:239], v[20:23], v[52:55], v[236:239]
	v_mfma_f32_16x16x32_f16 v[240:243], v[24:27], v[52:55], v[240:243]
	v_mfma_f32_16x16x32_f16 v[244:247], v[28:31], v[52:55], v[244:247]
	v_mfma_f32_16x16x32_f16 v[248:251], v[32:35], v[52:55], v[248:251]
	v_mfma_f32_16x16x32_f16 v[252:255], v[36:39], v[52:55], v[252:255]
	s_barrier
	s_add_u32 s21, s21, 1
	s_cmp_lt_u32 s21, 12
	s_cbranch_scc1 .Lfc_h0_loop
	s_barrier
	s_branch .Lfc_epi
.Lfc_h1_entry:
	s_setprio 1
	s_add_u32 m0, s22, 0x0
	s_nop 0
	global_load_lds_dwordx4 v5, s[24:25]
	s_add_u32 m0, s22, 0x400
	s_nop 0
	global_load_lds_dwordx4 v6, s[24:25]
	s_add_u32 m0, s23, 0x0
	s_nop 0
	global_load_lds_dwordx4 v11, s[28:29]
	s_add_u32 m0, s23, 0x400
	s_nop 0
	global_load_lds_dwordx4 v11, s[32:33]
	s_add_u32 m0, s23, 0x800
	s_nop 0
	global_load_lds_dwordx4 v11, s[36:37]
	s_add_u32 s24, s24, 0x80
	s_addc_u32 s25, s25, 0
	s_add_u32 s28, s28, 0x30000
	s_addc_u32 s29, s29, 0
	s_add_u32 s32, s32, 0x30000
	s_addc_u32 s33, s33, 0
	s_add_u32 s36, s36, 0x30000
	s_addc_u32 s37, s37, 0
	s_add_u32 m0, s22, 0xa000
	s_nop 0
	global_load_lds_dwordx4 v5, s[26:27]
	s_add_u32 m0, s22, 0xa400
	s_nop 0
	global_load_lds_dwordx4 v6, s[26:27]
	s_add_u32 m0, s23, 0xa000
	s_nop 0
	global_load_lds_dwordx4 v11, s[30:31]
	s_add_u32 m0, s23, 0xa400
	s_nop 0
	global_load_lds_dwordx4 v11, s[34:35]
	s_add_u32 m0, s23, 0xa800
	s_nop 0
	global_load_lds_dwordx4 v11, s[38:39]
	s_add_u32 s26, s26, 0x80
	s_addc_u32 s27, s27, 0
	s_add_u32 s30, s30, 0x30000
	s_addc_u32 s31, s31, 0
	s_add_u32 s34, s34, 0x30000
	s_addc_u32 s35, s35, 0
	s_add_u32 s38, s38, 0x30000
	s_addc_u32 s39, s39, 0
	s_add_u32 m0, s22, 0x14000
	s_nop 0
	global_load_lds_dwordx4 v5, s[24:25]
	s_add_u32 m0, s22, 0x14400
	s_nop 0
	global_load_lds_dwordx4 v6, s[24:25]
	s_add_u32 m0, s23, 0x14000
	s_nop 0
	global_load_lds_dwordx4 v11, s[28:29]
	s_add_u32 m0, s23, 0x14400
	s_nop 0
	global_load_lds_dwordx4 v11, s[32:33]
	s_add_u32 m0, s23, 0x14800
	s_nop 0
	global_load_lds_dwordx4 v11, s[36:37]
	s_add_u32 s24, s24, 0x80
	s_addc_u32 s25, s25, 0
	s_add_u32 s28, s28, 0x30000
	s_addc_u32 s29, s29, 0
	s_add_u32 s32, s32, 0x30000
	s_addc_u32 s33, s33, 0
	s_add_u32 s36, s36, 0x30000
	s_addc_u32 s37, s37, 0
	s_add_u32 m0, s22, 0x1e000
	s_nop 0
	global_load_lds_dwordx4 v5, s[26:27]
	s_add_u32 m0, s22, 0x1e400
	s_nop 0
	global_load_lds_dwordx4 v6, s[26:27]
	s_add_u32 m0, s23, 0x1e000
	s_nop 0
	global_load_lds_dwordx4 v11, s[30:31]
	s_add_u32 m0, s23, 0x1e400
	s_nop 0
	global_load_lds_dwordx4 v11, s[34:35]
	s_add_u32 m0, s23, 0x1e800
	s_nop 0
	global_load_lds_dwordx4 v11, s[38:39]
	s_add_u32 s26, s26, 0x80
	s_addc_u32 s27, s27, 0
	s_add_u32 s30, s30, 0x30000
	s_addc_u32 s31, s31, 0
	s_add_u32 s34, s34, 0x30000
	s_addc_u32 s35, s35, 0
	s_add_u32 s38, s38, 0x30000
	s_addc_u32 s39, s39, 0
	s_waitcnt vmcnt(20)
	v_med3_i32 v64, v64, 0, s93
	v_med3_i32 v65, v65, 1, s94
	v_med3_i32 v66, v66, 0, s93
	v_med3_i32 v67, v67, 1, s94
	v_add_u32_e32 v64, s92, v64
	v_add_u32_e32 v66, s92, v66
	v_add_u32_e32 v65, s92, v65
	v_add_u32_e32 v67, s92, v67
	v_add_u32_e32 v65, -1, v65
	v_add_u32_e32 v67, -1, v67
	v_lshl_add_u32 v7, v64, 10, v71
	v_lshl_add_u32 v8, v66, 10, v71
	v_lshl_add_u32 v9, v65, 10, v71
	v_lshl_add_u32 v10, v67, 10, v71
	v_cvt_pk_f16_f32 v12, v40, v41
	v_cvt_pk_f16_f32 v13, v42, v43
	v_cvt_pk_f16_f32 v14, v44, v45
	v_cvt_pk_f16_f32 v15, v46, v47
	v_cvt_pk_f16_f32 v56, v56, v57
	v_cvt_pk_f16_f32 v57, v58, v59
	v_cvt_pk_f16_f32 v58, v60, v61
	v_cvt_pk_f16_f32 v59, v62, v63
	v_cvt_pk_f16_f32 v60, v48, v49
	v_cvt_pk_f16_f32 v61, v50, v51
	v_cvt_pk_f16_f32 v62, v52, v53
	v_cvt_pk_f16_f32 v63, v54, v55
	v_mov_b32_e32 v64, v16
	v_mov_b32_e32 v65, v17
	v_mov_b32_e32 v66, v18
	v_mov_b32_e32 v67, v19
	v_mov_b32_e32 v68, v20
	v_mov_b32_e32 v69, v21
	v_mov_b32_e32 v70, v22
	v_mov_b32_e32 v71, v23
	v_mov_b32_e32 v72, v24
	v_mov_b32_e32 v73, v25
	v_mov_b32_e32 v74, v26
	v_mov_b32_e32 v75, v27
	v_mov_b32_e32 v76, v28
	v_mov_b32_e32 v77, v29
	v_mov_b32_e32 v78, v30
	v_mov_b32_e32 v79, v31
	v_mov_b32_e32 v80, v32
	v_mov_b32_e32 v81, v33
	v_mov_b32_e32 v82, v34
	v_mov_b32_e32 v83, v35
	v_mov_b32_e32 v84, v36
	v_mov_b32_e32 v85, v37
	v_mov_b32_e32 v86, v38
	v_mov_b32_e32 v87, v39
	v_mov_b32_e32 v88, v16
	v_mov_b32_e32 v89, v17
	v_mov_b32_e32 v90, v18
	v_mov_b32_e32 v91, v19
	v_mov_b32_e32 v92, v20
	v_mov_b32_e32 v93, v21
	v_mov_b32_e32 v94, v22
	v_mov_b32_e32 v95, v23
	v_mov_b32_e32 v96, v24
	v_mov_b32_e32 v97, v25
	v_mov_b32_e32 v98, v26
	v_mov_b32_e32 v99, v27
	v_mov_b32_e32 v100, v28
	v_mov_b32_e32 v101, v29
	v_mov_b32_e32 v102, v30
	v_mov_b32_e32 v103, v31
	v_mov_b32_e32 v104, v32
	v_mov_b32_e32 v105, v33
	v_mov_b32_e32 v106, v34
	v_mov_b32_e32 v107, v35
	v_mov_b32_e32 v108, v36
	v_mov_b32_e32 v109, v37
	v_mov_b32_e32 v110, v38
	v_mov_b32_e32 v111, v39
	v_mov_b32_e32 v112, v16
	v_mov_b32_e32 v113, v17
	v_mov_b32_e32 v114, v18
	v_mov_b32_e32 v115, v19
	v_mov_b32_e32 v116, v20
	v_mov_b32_e32 v117, v21
	v_mov_b32_e32 v118, v22
	v_mov_b32_e32 v119, v23
	v_mov_b32_e32 v120, v24
	v_mov_b32_e32 v121, v25
	v_mov_b32_e32 v122, v26
	v_mov_b32_e32 v123, v27
	v_mov_b32_e32 v124, v28
	v_mov_b32_e32 v125, v29
	v_mov_b32_e32 v126, v30
	v_mov_b32_e32 v127, v31
	v_mov_b32_e32 v128, v32
	v_mov_b32_e32 v129, v33
	v_mov_b32_e32 v130, v34
	v_mov_b32_e32 v131, v35
	v_mov_b32_e32 v132, v36
	v_mov_b32_e32 v133, v37
	v_mov_b32_e32 v134, v38
	v_mov_b32_e32 v135, v39
	v_mov_b32_e32 v136, v16
	v_mov_b32_e32 v137, v17
	v_mov_b32_e32 v138, v18
	v_mov_b32_e32 v139, v19
	v_mov_b32_e32 v140, v20
	v_mov_b32_e32 v141, v21
	v_mov_b32_e32 v142, v22
	v_mov_b32_e32 v143, v23
	v_mov_b32_e32 v144, v24
	v_mov_b32_e32 v145, v25
	v_mov_b32_e32 v146, v26
	v_mov_b32_e32 v147, v27
	v_mov_b32_e32 v148, v28
	v_mov_b32_e32 v149, v29
	v_mov_b32_e32 v150, v30
	v_mov_b32_e32 v151, v31
	v_mov_b32_e32 v152, v32
	v_mov_b32_e32 v153, v33
	v_mov_b32_e32 v154, v34
	v_mov_b32_e32 v155, v35
	v_mov_b32_e32 v156, v36
	v_mov_b32_e32 v157, v37
	v_mov_b32_e32 v158, v38
	v_mov_b32_e32 v159, v39
	v_mov_b32_e32 v160, v16
	v_mov_b32_e32 v161, v17
	v_mov_b32_e32 v162, v18
	v_mov_b32_e32 v163, v19
	v_mov_b32_e32 v164, v20
	v_mov_b32_e32 v165, v21
	v_mov_b32_e32 v166, v22
	v_mov_b32_e32 v167, v23
	v_mov_b32_e32 v168, v24
	v_mov_b32_e32 v169, v25
	v_mov_b32_e32 v170, v26
	v_mov_b32_e32 v171, v27
	v_mov_b32_e32 v172, v28
	v_mov_b32_e32 v173, v29
	v_mov_b32_e32 v174, v30
	v_mov_b32_e32 v175, v31
	v_mov_b32_e32 v176, v32
	v_mov_b32_e32 v177, v33
	v_mov_b32_e32 v178, v34
	v_mov_b32_e32 v179, v35
	v_mov_b32_e32 v180, v36
	v_mov_b32_e32 v181, v37
	v_mov_b32_e32 v182, v38
	v_mov_b32_e32 v183, v39
	v_mov_b32_e32 v184, v16
	v_mov_b32_e32 v185, v17
	v_mov_b32_e32 v186, v18
	v_mov_b32_e32 v187, v19
	v_mov_b32_e32 v188, v20
	v_mov_b32_e32 v189, v21
	v_mov_b32_e32 v190, v22
	v_mov_b32_e32 v191, v23
	v_mov_b32_e32 v192, v24
	v_mov_b32_e32 v193, v25
	v_mov_b32_e32 v194, v26
	v_mov_b32_e32 v195, v27
	v_mov_b32_e32 v196, v28
	v_mov_b32_e32 v197, v29
	v_mov_b32_e32 v198, v30
	v_mov_b32_e32 v199, v31
	v_mov_b32_e32 v200, v32
	v_mov_b32_e32 v201, v33
	v_mov_b32_e32 v202, v34
	v_mov_b32_e32 v203, v35
	v_mov_b32_e32 v204, v36
	v_mov_b32_e32 v205, v37
	v_mov_b32_e32 v206, v38
	v_mov_b32_e32 v207, v39
	v_mov_b32_e32 v208, v16
	v_mov_b32_e32 v209, v17
	v_mov_b32_e32 v210, v18
	v_mov_b32_e32 v211, v19
	v_mov_b32_e32 v212, v20
	v_mov_b32_e32 v213, v21
	v_mov_b32_e32 v214, v22
	v_mov_b32_e32 v215, v23
	v_mov_b32_e32 v216, v24
	v_mov_b32_e32 v217, v25
	v_mov_b32_e32 v218, v26
	v_mov_b32_e32 v219, v27
	v_mov_b32_e32 v220, v28
	v_mov_b32_e32 v221, v29
	v_mov_b32_e32 v222, v30
	v_mov_b32_e32 v223, v31
	v_mov_b32_e32 v224, v32
	v_mov_b32_e32 v225, v33
	v_mov_b32_e32 v226, v34
	v_mov_b32_e32 v227, v35
	v_mov_b32_e32 v228, v36
	v_mov_b32_e32 v229, v37
	v_mov_b32_e32 v230, v38
	v_mov_b32_e32 v231, v39
	v_mov_b32_e32 v232, v16
	v_mov_b32_e32 v233, v17
	v_mov_b32_e32 v234, v18
	v_mov_b32_e32 v235, v19
	v_mov_b32_e32 v236, v20
	v_mov_b32_e32 v237, v21
	v_mov_b32_e32 v238, v22
	v_mov_b32_e32 v239, v23
	v_mov_b32_e32 v240, v24
	v_mov_b32_e32 v241, v25
	v_mov_b32_e32 v242, v26
	v_mov_b32_e32 v243, v27
	v_mov_b32_e32 v244, v28
	v_mov_b32_e32 v245, v29
	v_mov_b32_e32 v246, v30
	v_mov_b32_e32 v247, v31
	v_mov_b32_e32 v248, v32
	v_mov_b32_e32 v249, v33
	v_mov_b32_e32 v250, v34
	v_mov_b32_e32 v251, v35
	v_mov_b32_e32 v252, v36
	v_mov_b32_e32 v253, v37
	v_mov_b32_e32 v254, v38
	v_mov_b32_e32 v255, v39
	s_waitcnt vmcnt(15)
	s_barrier
	s_barrier
.Lfc_h1_loop:
	ds_read_b128 v[16:19], v3 offset:0
	ds_read_b128 v[20:23], v3 offset:1024
	ds_read_b128 v[24:27], v3 offset:2048
	ds_read_b128 v[28:31], v3 offset:3072
	ds_read_b128 v[32:35], v3 offset:4096
	ds_read_b128 v[36:39], v3 offset:5120
	ds_read_b128 v[40:43], v1 offset:0
	ds_read_b128 v[44:47], v1 offset:1024
	ds_read_b128 v[48:51], v1 offset:2048
	ds_read_b128 v[52:55], v1 offset:3072
	s_cmp_eq_u32 s21, 0
	s_cbranch_scc1 .Lfc_ng_10
	s_add_u32 m0, s22, 0x1e000
	s_nop 0
	global_load_lds_dwordx4 v5, s[26:27]
	s_add_u32 m0, s22, 0x1e400
	s_nop 0
	global_load_lds_dwordx4 v6, s[26:27]
	s_add_u32 m0, s23, 0x1e000
	s_nop 0
	global_load_lds_dwordx4 v11, s[30:31]
	s_add_u32 m0, s23, 0x1e400
	s_nop 0
	global_load_lds_dwordx4 v11, s[34:35]
	s_add_u32 m0, s23, 0x1e800
	s_nop 0
	global_load_lds_dwordx4 v11, s[38:39]
	s_add_u32 s26, s26, 0x80
	s_addc_u32 s27, s27, 0
	s_add_u32 s30, s30, 0x30000
	s_addc_u32 s31, s31, 0
	s_add_u32 s34, s34, 0x30000
	s_addc_u32 s35, s35, 0
	s_add_u32 s38, s38, 0x30000
	s_addc_u32 s39, s39, 0
	s_cmp_eq_u32 s21, 3
	s_cbranch_scc1 .Lfc_sw_11
	s_cmp_eq_u32 s21, 7
	s_cbranch_scc0 .Lfc_swd_11
	s_add_u32 s28, s28, 0x180000
	s_addc_u32 s29, s29, 0
	s_add_u32 s30, s30, 0x180000
	s_addc_u32 s31, s31, 0
	s_add_u32 s32, s32, 0x180000
	s_addc_u32 s33, s33, 0
	s_add_u32 s34, s34, 0x180000
	s_addc_u32 s35, s35, 0
	s_add_u32 s36, s36, 0x180000
	s_addc_u32 s37, s37, 0
	s_add_u32 s38, s38, 0x180000
	s_addc_u32 s39, s39, 0
	s_branch .Lfc_sw2_11
